# converter queue: two quarter-strips per atomic pull (half the pulls on the shared counter, one drain per two items)
# baseline (speedup 1.0000x reference)
; #define GAS __attribute__((address_space(1)))
; #define P0_GET() do { if (DYN) { int v_ = 0x7fffffff; if (lane == 0) { if (!check_stop || __hip_atomic_load(stopw, RLX_AGENT) == 0u) v_ = (int)atomicAdd(qword, 1u); } \
;         idx = __builtin_amdgcn_readfirstlane(v_); ok = idx < P0_NHALF; } else { idx = cur_static; cur_static += nw; ok = idx < s1; } } while (0)
; #define P0_MAKE() (DYN ? p0_strip_half(args, ws, idx) : p0_strip(args, ws, idx))
; #define P0_LD(B_) do { if (lv) { p0_load(B_, lst, lj, lane); if (++lj == lst.nk) { lj = 0; P0_GET(); if (ok) { lst = P0_MAKE(); nst = lst; has_n = true; } else lv = false; } } } while (0)
; __device__ __forceinline__ void p0_load(f32x4 (&v)[8], const Strip& st, int j, int lane) {
;     const float* p = st.src + (size_t)(j * 64 + (lane >> 3)) * st.ldw + (lane & 7) * 4;
; #pragma unroll
;     for (int i = 0; i < 8; ++i) v[i] = __builtin_nontemporal_load((const GAS f32x4*)(p + (size_t)(i * 8) * st.ldw));
; }
; template <bool DYN>
; __device__ __forceinline__ void p0_walk(const Args& args, unsigned char* ws, LAS float* scr, int lane, int w, int nw, int s0, int s1, unsigned* qword, unsigned* stopw, bool check_stop) {
;     ...
;     P0_GET();
;     if (!ok) return;
;     Strip lst = P0_MAKE(), sst = lst, nst = lst; bool has_n = false, lv = true, sv = true; int lj = 0, sj = 0;
;     f32x4 b0[8], b1[8], b2[8], b3[8]; u32x2 hold[4];
;     ...
;     P0_LD(b0); P0_LD(b1); P0_LD(b2);
.LBB0_33:
	s_lshl_b32 s17, s17, 5
	s_lshl_b32 s22, s74, 14
	s_and_b32 s17, s17, 0x7e0
	s_add_i32 s22, s22, 0
	s_lshl_b32 s23, s17, 2
	s_add_u32 s23, s38, s23
	s_addc_u32 s26, s39, 0
	s_lshl_b32 s3, s3, 9
	s_and_b32 s3, s3, 0x600
	s_lshl_b32 s27, s3, 13
	s_add_u32 s44, s23, s27
	v_lshrrev_b32_e32 v133, 3, v164
	s_addc_u32 s45, s26, 0
	v_lshlrev_b32_e32 v130, 13, v133
	v_mov_b32_e32 v131, 0
	v_and_b32_e32 v132, 28, v166
	v_lshl_add_u64 v[2:3], s[44:45], 0, v[130:131]
	v_lshlrev_b32_e32 v130, 2, v132
	v_lshl_add_u64 v[74:75], v[2:3], 0, v[130:131]
	s_mov_b32 s23, 0x10000
	v_add_co_u32_e32 v6, vcc, s23, v74
	s_mov_b32 s23, 0x20000
	s_nop 0
	v_addc_co_u32_e32 v7, vcc, 0, v75, vcc
	v_add_co_u32_e32 v10, vcc, s23, v74
	s_mov_b32 s23, 0x30000
	s_nop 0
	v_addc_co_u32_e32 v11, vcc, 0, v75, vcc
	v_add_co_u32_e32 v14, vcc, s23, v74
	s_mov_b32 s23, 0x40000
	s_nop 0
	v_addc_co_u32_e32 v15, vcc, 0, v75, vcc
	v_add_co_u32_e32 v18, vcc, s23, v74
	s_mov_b32 s23, 0x50000
	s_nop 0
	v_addc_co_u32_e32 v19, vcc, 0, v75, vcc
	v_add_co_u32_e32 v22, vcc, s23, v74
	s_mov_b32 s23, 0x60000
	s_nop 0
	v_addc_co_u32_e32 v23, vcc, 0, v75, vcc
	v_add_co_u32_e32 v26, vcc, s23, v74
	s_mov_b32 s23, 0x70000
	s_nop 0
	v_addc_co_u32_e32 v27, vcc, 0, v75, vcc
	v_add_co_u32_e32 v30, vcc, s23, v74
	s_mov_b32 s23, 0x80000
	s_nop 0
	v_addc_co_u32_e32 v31, vcc, 0, v75, vcc
	v_add_co_u32_e32 v34, vcc, s23, v74
	s_mov_b32 s23, 0x90000
	s_nop 0
	v_addc_co_u32_e32 v35, vcc, 0, v75, vcc
	v_add_co_u32_e32 v38, vcc, s23, v74
	s_mov_b32 s23, 0xa0000
	s_nop 0
	v_addc_co_u32_e32 v39, vcc, 0, v75, vcc
	v_add_co_u32_e32 v42, vcc, s23, v74
	s_mov_b32 s23, 0xb0000
	s_nop 0
	v_addc_co_u32_e32 v43, vcc, 0, v75, vcc
	v_add_co_u32_e32 v46, vcc, s23, v74
	s_mov_b32 s23, 0xc0000
	s_nop 0
	v_addc_co_u32_e32 v47, vcc, 0, v75, vcc
	v_add_co_u32_e32 v50, vcc, s23, v74
	s_mov_b32 s23, 0xd0000
	s_nop 0
	v_addc_co_u32_e32 v51, vcc, 0, v75, vcc
	v_add_co_u32_e32 v54, vcc, s23, v74
	s_mov_b32 s23, 0xe0000
	s_nop 0
	v_addc_co_u32_e32 v55, vcc, 0, v75, vcc
	v_add_co_u32_e32 v58, vcc, s23, v74
	s_mov_b32 s23, 0xf0000
	s_nop 0
	v_addc_co_u32_e32 v59, vcc, 0, v75, vcc
	v_add_co_u32_e32 v62, vcc, s23, v74
	s_mov_b32 s23, 0x100000
	s_nop 0
	v_addc_co_u32_e32 v63, vcc, 0, v75, vcc
	v_add_co_u32_e32 v66, vcc, s23, v74
	s_mov_b32 s23, 0x110000
	s_nop 0
	v_addc_co_u32_e32 v67, vcc, 0, v75, vcc
	v_add_co_u32_e32 v70, vcc, s23, v74
	s_mov_b32 s23, 0x120000
	s_nop 0
	v_addc_co_u32_e32 v71, vcc, 0, v75, vcc
	v_add_co_u32_e32 v76, vcc, s23, v74
	s_mov_b32 s23, 0x130000
	s_nop 0
	v_addc_co_u32_e32 v77, vcc, 0, v75, vcc
	v_add_co_u32_e32 v78, vcc, s23, v74
	s_mov_b32 s23, 0x140000
	s_nop 0
	v_addc_co_u32_e32 v79, vcc, 0, v75, vcc
	global_load_dwordx4 v[2:5], v[74:75], off nt
	s_nop 0
	global_load_dwordx4 v[6:9], v[6:7], off nt
	s_nop 0
	global_load_dwordx4 v[10:13], v[10:11], off nt
	s_nop 0
	global_load_dwordx4 v[14:17], v[14:15], off nt
	s_nop 0
	global_load_dwordx4 v[18:21], v[18:19], off nt
	s_nop 0
	global_load_dwordx4 v[22:25], v[22:23], off nt
	s_nop 0
	global_load_dwordx4 v[26:29], v[26:27], off nt
	s_nop 0
	global_load_dwordx4 v[30:33], v[30:31], off nt
	s_nop 0
	global_load_dwordx4 v[34:37], v[34:35], off nt
	s_nop 0
	global_load_dwordx4 v[38:41], v[38:39], off nt
	s_nop 0
	global_load_dwordx4 v[42:45], v[42:43], off nt
	s_nop 0
	global_load_dwordx4 v[46:49], v[46:47], off nt
	s_nop 0
	global_load_dwordx4 v[50:53], v[50:51], off nt
	s_nop 0
	global_load_dwordx4 v[54:57], v[54:55], off nt
	s_nop 0
	global_load_dwordx4 v[58:61], v[58:59], off nt
	s_nop 0
	global_load_dwordx4 v[62:65], v[62:63], off nt
	s_nop 0
	global_load_dwordx4 v[66:69], v[66:67], off nt
	s_nop 0
	global_load_dwordx4 v[70:73], v[70:71], off nt
	s_nop 0
	global_load_dwordx4 v[82:85], v[76:77], off nt
	global_load_dwordx4 v[86:89], v[78:79], off nt
	v_add_co_u32_e32 v76, vcc, s23, v74
	s_mov_b32 s23, 0x150000
	s_nop 0
	v_addc_co_u32_e32 v77, vcc, 0, v75, vcc
	v_add_co_u32_e32 v78, vcc, s23, v74
	s_mov_b32 s23, 0x160000
	s_nop 0
	v_addc_co_u32_e32 v79, vcc, 0, v75, vcc
	global_load_dwordx4 v[98:101], v[76:77], off nt
	global_load_dwordx4 v[102:105], v[78:79], off nt
	v_add_co_u32_e32 v76, vcc, s23, v74
	s_mov_b32 s23, 0x170000
	s_nop 0
	v_addc_co_u32_e32 v77, vcc, 0, v75, vcc
	v_add_co_u32_e32 v74, vcc, s23, v74
	s_add_u32 s42, s10, s3
	s_nop 0
	v_addc_co_u32_e32 v75, vcc, 0, v75, vcc
	global_load_dwordx4 v[114:117], v[76:77], off nt
	global_load_dwordx4 v[122:125], v[74:75], off nt
	s_addc_u32 s43, s11, 0
	s_load_dwordx2 s[10:11], s[0:1], 0x78
	s_load_dwordx2 s[38:39], s[0:1], 0x88
	s_load_dwordx2 s[40:41], s[0:1], 0x98
	v_and_b32_e32 v76, 7, v0
	v_add_u32_e32 v74, s22, v130
	v_mul_u32_u24_e32 v75, 0x84, v133
	v_lshlrev_b32_e32 v134, 3, v76
	v_mul_u32_u24_e32 v76, 0x420, v76
	v_lshlrev_b32_e32 v77, 2, v133
	s_mov_b32 s26, 0
	s_mov_b32 s3, 3
	v_or_b32_e32 v165, 8, v133
	v_or_b32_e32 v167, 16, v133
	v_or_b32_e32 v182, 24, v133
	v_mov_b32_e32 v135, v131
	v_add3_u32 v183, s22, v76, v77
	s_mov_b64 s[48:49], -1
	s_mov_b64 s[52:53], 0
	s_movk_i32 s60, 0x2000
	s_mov_b32 s61, 0x7fffff00
	s_movk_i32 s62, 0x7f
	s_movk_i32 s63, 0x80
	s_mov_b32 s64, 0xaaaaaaab
	s_movk_i32 s65, 0xc0
	s_movk_i32 s66, 0x3ff
	s_movk_i32 s67, 0x440
	v_add_u32_e32 v184, v74, v75
	s_mov_b64 s[46:47], s[42:43]
	s_mov_b32 s68, s16
	s_mov_b32 s69, s17
	v_mov_b32_e32 v255, 0
	s_mov_b32 s101, 0
	s_branch .LBB0_35

; #define P0_GET() do { if (DYN) { int v_ = 0x7fffffff; if (lane == 0) { if (!check_stop || __hip_atomic_load(stopw, RLX_AGENT) == 0u) v_ = (int)atomicAdd(qword, 1u); } \
;         idx = __builtin_amdgcn_readfirstlane(v_); ok = idx < P0_NHALF; } else { idx = cur_static; cur_static += nw; ok = idx < s1; } } while (0)
; #define P0_MAKE() (DYN ? p0_strip_half(args, ws, idx) : p0_strip(args, ws, idx))
; template <bool DYN>
; __device__ __forceinline__ void p0_walk(const Args& args, unsigned char* ws, LAS float* scr, int lane, int w, int nw, int s0, int s1, unsigned* qword, unsigned* stopw, bool check_stop) {
;     ...
;     P0_GET();
;     if (!ok) return;
;     Strip lst = P0_MAKE(), sst = lst, nst = lst; bool has_n = false, lv = true, sv = true; int lj = 0, sj = 0;
;     f32x4 b0[8], b1[8], b2[8], b3[8]; u32x2 hold[4];
.LBB0_35:
	s_andn2_b64 vcc, exec, s[48:49]
	s_cbranch_vccnz .LBB0_53
	v_lshl_or_b32 v130, s3, 6, v133
	v_lshlrev_b64 v[74:75], 13, v[130:131]
	v_lshl_add_u64 v[74:75], s[44:45], 0, v[74:75]
	v_lshlrev_b32_e32 v130, 2, v132
	v_lshl_add_u64 v[118:119], v[74:75], 0, v[130:131]
	v_add_co_u32_e32 v78, vcc, 0x10000, v118
	s_add_i32 s3, s3, 1
	s_nop 0
	v_addc_co_u32_e32 v79, vcc, 0, v119, vcc
	v_add_co_u32_e32 v90, vcc, 0x20000, v118
	global_load_dwordx4 v[74:77], v[118:119], off nt
	s_nop 0
	global_load_dwordx4 v[78:81], v[78:79], off nt
	v_addc_co_u32_e32 v91, vcc, 0, v119, vcc
	v_add_co_u32_e32 v94, vcc, 0x30000, v118
	s_cmp_lg_u32 s3, 8
	s_nop 0
	v_addc_co_u32_e32 v95, vcc, 0, v119, vcc
	v_add_co_u32_e32 v106, vcc, 0x40000, v118
	global_load_dwordx4 v[90:93], v[90:91], off nt
	s_nop 0
	global_load_dwordx4 v[94:97], v[94:95], off nt
	v_addc_co_u32_e32 v107, vcc, 0, v119, vcc
	v_add_co_u32_e32 v110, vcc, 0x50000, v118
	s_mov_b64 s[48:49], -1
	s_nop 0
	v_addc_co_u32_e32 v111, vcc, 0, v119, vcc
	v_add_co_u32_e32 v120, vcc, 0x60000, v118
	global_load_dwordx4 v[106:109], v[106:107], off nt
	s_nop 0
	global_load_dwordx4 v[110:113], v[110:111], off nt
	v_addc_co_u32_e32 v121, vcc, 0, v119, vcc
	v_add_co_u32_e32 v126, vcc, 0x70000, v118
	s_nop 1
	v_addc_co_u32_e32 v127, vcc, 0, v119, vcc
	global_load_dwordx4 v[118:121], v[120:121], off nt
	s_nop 0
	global_load_dwordx4 v[126:129], v[126:127], off nt
	s_cbranch_scc1 .LBB0_54
	s_cmp_eq_u32 s101, 0
	s_cbranch_scc1 .Lcvq_pull
	s_mov_b32 s101, 0
	s_mov_b32 s3, s100
	s_branch .Lcvq_have
.Lcvq_pull:
	v_bfrev_b32_e32 v130, -2
	s_and_saveexec_b64 s[48:49], s[4:5]
	s_cbranch_execz .LBB0_42
	v_mov_b32_e32 v130, v255
	global_load_dword v255, v131, s[6:7] sc1
	v_cmp_ne_u32_e32 vcc, 0, v130
	v_bfrev_b32_e32 v130, -2
	s_cbranch_vccnz .LBB0_42
	s_mov_b64 s[54:55], exec
	v_mbcnt_lo_u32_b32 v130, s54, 0
	v_mbcnt_hi_u32_b32 v130, s55, v130
	v_cmp_eq_u32_e32 vcc, 0, v130
	s_and_saveexec_b64 s[50:51], vcc
	s_cbranch_execz .LBB0_41
	s_bcnt1_i32_b64 s3, s[54:55]
	s_lshl_b32 s3, s3, 1
	s_waitcnt lgkmcnt(0)
	v_mov_b32_e32 v136, s3
	global_atomic_add v136, v131, v136, s[8:9] sc0

; __device__ __forceinline__ Strip p0_strip_half(const Args& args, unsigned char* ws, int q) {
;     Strip st = p0_strip(args, ws, q >> 2); st.nk = 8; st.src += (size_t)(q & 3) * 512 * st.ldw; st.dst += (size_t)(q & 3) * 512; return st;
.LBB0_42:
	s_or_b64 exec, exec, s[48:49]
	v_readfirstlane_b32 s3, v130
	s_nop 3
	s_add_i32 s100, s3, 1
	s_cmpk_gt_i32 s3, 0x5fff
	s_cselect_b32 s101, 0, 1
.Lcvq_have:
	s_cmpk_gt_i32 s3, 0x5fff
	s_mov_b64 s[48:49], 0
	s_cbranch_scc1 .LBB0_52
	s_ashr_i32 s27, s3, 2
	s_bfe_u32 s50, s27, 0x50006
	s_cmpk_gt_u32 s27, 0x7ff
	s_mov_b64 s[48:49], -1
	s_cbranch_scc0 .LBB0_49
	s_and_b32 s22, s3, 0xffffe000
	s_cmpk_lg_i32 s22, 0x2000
	s_cbranch_scc0 .LBB0_46
	s_lshl_b32 s22, s50, 22
	s_lshl_b32 s23, s50, 24
	s_waitcnt lgkmcnt(0)
	s_add_u32 s44, s40, s23
	s_addc_u32 s45, s41, 0
	v_readlane_b32 s23, v252, 3
	s_add_u32 s46, s23, s22
	s_addc_u32 s47, s84, 0
	s_mov_b64 s[48:49], 0
